# FoX tile loop: cum-slot reads issued behind the tile barrier; first three K fragments read ahead of the bias subtraction on the unmasked path
# baseline (speedup 1.0000x reference)
.LBB0_415:
	s_add_i32 s14, s65, 0x42
	s_min_u32 s14, s14, s40
	s_mul_i32 s52, s14, 0xc0000
	s_mul_hi_u32 s53, s14, 0xc0000
	s_add_u32 s48, s0, s52
	s_mul_i32 s67, s66, 0x8800
	s_addc_u32 s49, s1, s53
	s_add_i32 s54, s67, 0xffff7800
	s_cmp_gt_i32 s66, 0
	s_cselect_b32 s54, s54, 0x11000
	s_add_i32 s54, s54, 0
	s_add_u32 s52, s2, s52
	s_addc_u32 s53, s3, s53
	s_add_i32 s55, s54, s59
	s_waitcnt vmcnt(5) lgkmcnt(0)
	s_barrier
	s_add_i32 s32, s23, s67
	v_add_u32_e32 v169, s32, v159
	ds_read_b128 v[110:113], v169 offset:32768
	ds_read_b128 v[118:121], v169 offset:32832
	ds_read_b128 v[130:133], v169 offset:32896
	ds_read_b128 v[134:137], v169 offset:32960
	v_lshl_add_u64 v[106:107], s[48:49], 0, v[146:147]
	s_mov_b32 m0, s55
	s_lshl_b32 s14, s14, 6
	global_load_lds_dwordx4 v[106:107], off
	v_lshl_add_u64 v[106:107], s[52:53], 0, v[148:149]
	s_add_i32 m0, s55, 0x4000
	s_nop 0
	global_load_lds_dwordx4 v[106:107], off
	v_lshl_add_u64 v[106:107], s[48:49], 0, v[152:153]
	s_add_i32 s48, s54, s62
	s_mov_b32 m0, s48
	s_nop 0
	global_load_lds_dwordx4 v[106:107], off
	v_lshl_add_u64 v[106:107], s[52:53], 0, v[154:155]
	s_add_i32 m0, s48, 0x4000
	s_nop 0
	global_load_lds_dwordx4 v[106:107], off
	v_lshl_add_u64 v[106:107], s[14:15], 2, v[156:157]
	s_add_i32 s14, s54, s63
	s_add_i32 m0, s14, 0x8000
	s_cmp_gt_i32 s56, s41
	global_load_lds_dword v[106:107], off
	s_cbranch_scc1 .LBB0_414
	s_add_i32 s14, s56, 63
	s_add_i32 s52, s23, s67
	s_cmp_gt_i32 s14, s38
	v_sub_f32_e32 v160, v143, v167
	s_mov_b64 s[48:49], -1
	v_add_u32_e32 v169, s52, v159
	v_sub_f32_e32 v158, v151, v168
	s_cbranch_scc1 .LBB0_418
	v_add_u32_e32 v250, s67, v161
	v_add_u32_e32 v251, v250, v162
	ds_read_b128 v[170:173], v251 offset:0
	v_add_u32_e32 v230, v250, v163
	ds_read_b128 v[174:177], v230 offset:0
	v_add_u32_e32 v231, v250, v164
	ds_read_b128 v[178:181], v231 offset:0
	s_mov_b64 s[48:49], 0
	s_waitcnt lgkmcnt(3)
	v_sub_f32_e32 v109, v160, v113
	v_sub_f32_e32 v108, v160, v112
	v_sub_f32_e32 v107, v160, v111
	v_sub_f32_e32 v106, v160, v110
	v_sub_f32_e32 v117, v160, v121
	v_sub_f32_e32 v116, v160, v120
	v_sub_f32_e32 v115, v160, v119
	v_sub_f32_e32 v114, v160, v118
	v_sub_f32_e32 v125, v160, v133
	v_sub_f32_e32 v124, v160, v132
	v_sub_f32_e32 v123, v160, v131
	v_sub_f32_e32 v122, v160, v130
	v_sub_f32_e32 v129, v160, v137
	v_sub_f32_e32 v128, v160, v136
	v_sub_f32_e32 v127, v160, v135
	v_sub_f32_e32 v126, v160, v134
	v_sub_f32_e32 v113, v158, v113
	v_sub_f32_e32 v112, v158, v112
	v_sub_f32_e32 v111, v158, v111
	v_sub_f32_e32 v110, v158, v110
	v_sub_f32_e32 v121, v158, v121
	v_sub_f32_e32 v120, v158, v120
	v_sub_f32_e32 v119, v158, v119
	v_sub_f32_e32 v118, v158, v118
	v_sub_f32_e32 v133, v158, v133
	v_sub_f32_e32 v132, v158, v132
	v_sub_f32_e32 v131, v158, v131
	v_sub_f32_e32 v130, v158, v130
	v_sub_f32_e32 v137, v158, v137
	v_sub_f32_e32 v136, v158, v136
	v_sub_f32_e32 v135, v158, v135
	v_sub_f32_e32 v134, v158, v134
	v_mov_b32_e32 v158, v250
	v_mov_b32_e32 v160, v251
	v_mov_b32_e32 v169, v230
	v_mov_b32_e32 v186, v231
	s_branch .Lfox_k3

.Lfox_k3:
	s_waitcnt lgkmcnt(2)
	v_add_u32_e32 v158, v158, v165
	v_mfma_f32_16x16x32_bf16 v[106:109], v[170:173], v[30:33], v[106:109]
	v_mfma_f32_16x16x32_bf16 v[110:113], v[170:173], v[50:53], v[110:113]
	ds_read_b128 v[170:173], v158 offset:0
	s_waitcnt lgkmcnt(2)
	v_mfma_f32_16x16x32_bf16 v[106:109], v[174:177], v[34:37], v[106:109]
	v_mfma_f32_16x16x32_bf16 v[110:113], v[174:177], v[54:57], v[110:113]
	ds_read_b128 v[174:177], v160 offset:0x1000
	s_waitcnt lgkmcnt(2)
	v_mfma_f32_16x16x32_bf16 v[106:109], v[178:181], v[38:41], v[106:109]
	ds_read_b128 v[182:185], v169 offset:0x1000
	s_waitcnt lgkmcnt(2)
	v_mfma_f32_16x16x32_bf16 v[178:181], v[178:181], v[58:61], v[110:113]
	v_mfma_f32_16x16x32_bf16 v[110:113], v[170:173], v[46:49], v[106:109]
	v_mfma_f32_16x16x32_bf16 v[106:109], v[170:173], v[62:65], v[178:181]
	ds_read_b128 v[170:173], v186 offset:0x1000
	s_waitcnt lgkmcnt(2)
	v_mfma_f32_16x16x32_bf16 v[114:117], v[174:177], v[30:33], v[114:117]
	v_mfma_f32_16x16x32_bf16 v[118:121], v[174:177], v[50:53], v[118:121]
	ds_read_b128 v[174:177], v158 offset:0x1000
	s_waitcnt lgkmcnt(2)
	v_mfma_f32_16x16x32_bf16 v[114:117], v[182:185], v[34:37], v[114:117]
	ds_read_b128 v[178:181], v160 offset:0x2000
	s_waitcnt lgkmcnt(2)
	v_mfma_f32_16x16x32_bf16 v[118:121], v[182:185], v[54:57], v[118:121]
	v_mfma_f32_16x16x32_bf16 v[114:117], v[170:173], v[38:41], v[114:117]
	ds_read_b128 v[182:185], v169 offset:0x2000
	s_waitcnt lgkmcnt(2)
	v_mfma_f32_16x16x32_bf16 v[170:173], v[170:173], v[58:61], v[118:121]
	v_mfma_f32_16x16x32_bf16 v[118:121], v[174:177], v[46:49], v[114:117]
	v_mfma_f32_16x16x32_bf16 v[114:117], v[174:177], v[62:65], v[170:173]
	ds_read_b128 v[170:173], v186 offset:0x2000
	s_waitcnt lgkmcnt(2)
	v_mfma_f32_16x16x32_bf16 v[122:125], v[178:181], v[30:33], v[122:125]
	ds_read_b128 v[174:177], v158 offset:0x2000
	s_waitcnt lgkmcnt(2)
	v_mfma_f32_16x16x32_bf16 v[130:133], v[178:181], v[50:53], v[130:133]
	v_mfma_f32_16x16x32_bf16 v[122:125], v[182:185], v[34:37], v[122:125]
	ds_read_b128 v[178:181], v160 offset:0x3000
	s_waitcnt lgkmcnt(2)
	v_mfma_f32_16x16x32_bf16 v[130:133], v[182:185], v[54:57], v[130:133]
	s_nop 1
	v_mfma_f32_16x16x32_bf16 v[122:125], v[170:173], v[38:41], v[122:125]
	ds_read_b128 v[182:185], v169 offset:0x3000
	s_waitcnt lgkmcnt(2)
	v_mfma_f32_16x16x32_bf16 v[170:173], v[170:173], v[58:61], v[130:133]
	v_mfma_f32_16x16x32_bf16 v[130:133], v[174:177], v[46:49], v[122:125]
	v_mfma_f32_16x16x32_bf16 v[122:125], v[174:177], v[62:65], v[170:173]
	ds_read_b128 v[170:173], v186 offset:0x3000
	s_waitcnt lgkmcnt(2)
	v_mfma_f32_16x16x32_bf16 v[126:129], v[178:181], v[30:33], v[126:129]
	ds_read_b128 v[174:177], v158 offset:0x3000
	s_waitcnt lgkmcnt(2)
	v_mfma_f32_16x16x32_bf16 v[134:137], v[178:181], v[50:53], v[134:137]
	v_mfma_f32_16x16x32_bf16 v[126:129], v[182:185], v[34:37], v[126:129]
	s_waitcnt lgkmcnt(1)
	v_mfma_f32_16x16x32_bf16 v[134:137], v[182:185], v[54:57], v[134:137]
	s_nop 1
	v_mfma_f32_16x16x32_bf16 v[126:129], v[170:173], v[38:41], v[126:129]
	s_waitcnt lgkmcnt(0)
	v_mfma_f32_16x16x32_bf16 v[170:173], v[170:173], v[58:61], v[134:137]
	v_and_b32_e32 v160, 64, v208
	v_xor_b32_e32 v158, 16, v208
	v_add_u32_e32 v160, 64, v160
	v_cmp_lt_i32_e32 vcc, v158, v160
	v_mfma_f32_16x16x32_bf16 v[134:137], v[174:177], v[46:49], v[126:129]
	s_mov_b64 s[48:49], 0
	v_cndmask_b32_e32 v158, v208, v158, vcc
	v_lshlrev_b32_e32 v169, 2, v158
	v_xor_b32_e32 v158, 32, v208
	v_cmp_lt_i32_e32 vcc, v158, v160
	v_mfma_f32_16x16x32_bf16 v[126:129], v[174:177], v[62:65], v[170:173]
	s_mov_b64 s[52:53], 0
	v_cndmask_b32_e32 v158, v208, v158, vcc
	s_nop 0
	v_lshlrev_b32_e32 v170, 2, v158
	v_max3_f32 v158, v110, s30, v111
	v_max3_f32 v158, v158, v112, v113
	v_max3_f32 v158, v158, v118, v119
	v_max3_f32 v158, v158, v120, v121
	v_max3_f32 v158, v158, v130, v131
	v_max3_f32 v158, v158, v132, v133
	v_max3_f32 v158, v158, v134, v135
	v_max3_f32 v158, v158, v136, v137
	v_max3_f32 v160, v106, s30, v107
	v_max3_f32 v160, v160, v108, v109
	v_max3_f32 v160, v160, v114, v115
	v_max3_f32 v160, v160, v116, v117
	v_max3_f32 v160, v160, v122, v123
	v_max3_f32 v160, v160, v124, v125
	v_max3_f32 v160, v160, v126, v127
	v_max3_f32 v160, v160, v128, v129
	v_mov_b32_e32 v230, v158
	v_mov_b32_e32 v231, v160
	s_nop 1
	v_permlane16_swap_b32 v230, v158
	v_permlane16_swap_b32 v231, v160
	v_max_f32_e32 v158, v158, v230
	v_max_f32_e32 v160, v160, v231
	v_mov_b32_e32 v230, v158
	v_mov_b32_e32 v231, v160
	s_nop 1
	v_permlane32_swap_b32 v230, v158
	v_permlane32_swap_b32 v231, v160
	v_max_f32_e32 v158, v158, v230
	v_max_f32_e32 v160, v160, v231
	v_cmp_lt_f32_e64 s[54:55], s31, v158
	v_cmp_lt_f32_e32 vcc, s34, v158
	s_orn2_b64 s[52:53], vcc, s[46:47]
	s_and_b64 s[52:53], s[52:53], s[54:55]
	v_cmp_lt_f32_e64 s[54:55], s31, v160
	v_cmp_lt_f32_e32 vcc, s34, v160
	s_orn2_b64 s[48:49], vcc, s[44:45]
	s_and_b64 s[48:49], s[48:49], s[54:55]
	s_or_b64 s[54:55], s[52:53], s[48:49]
	s_cbranch_scc0 .LBB0_413
	v_cndmask_b32_e64 v160, 0, v160, s[48:49]
	v_cndmask_b32_e64 v158, 0, v158, s[52:53]
	v_exp_f32_e64 v170, -v160
	v_exp_f32_e64 v169, -v158
	s_and_b64 vcc, s[48:49], s[44:45]
	s_or_b64 s[48:49], s[44:45], s[48:49]
	v_cndmask_b32_e32 v171, 1.0, v170, vcc
	s_and_b64 vcc, s[52:53], s[46:47]
	s_or_b64 s[52:53], s[46:47], s[52:53]
	v_add_f32_e32 v167, v167, v158
	v_sub_f32_e32 v110, v110, v158
	v_sub_f32_e32 v111, v111, v158
	v_sub_f32_e32 v112, v112, v158
	v_sub_f32_e32 v113, v113, v158
	v_sub_f32_e32 v118, v118, v158
	v_sub_f32_e32 v119, v119, v158
	v_sub_f32_e32 v120, v120, v158
	v_sub_f32_e32 v121, v121, v158
	v_sub_f32_e32 v130, v130, v158
	v_sub_f32_e32 v131, v131, v158
	v_sub_f32_e32 v132, v132, v158
	v_sub_f32_e32 v133, v133, v158
	v_sub_f32_e32 v134, v134, v158
	v_sub_f32_e32 v135, v135, v158
	v_sub_f32_e32 v136, v136, v158
	v_sub_f32_e32 v137, v137, v158
	v_cndmask_b32_e32 v170, 1.0, v169, vcc
	v_mov_b32_e32 v158, v171
	s_andn2_b64 s[46:47], s[46:47], exec
	s_and_b64 s[52:53], s[52:53], exec
	s_andn2_b64 s[44:45], s[44:45], exec
	s_and_b64 s[48:49], s[48:49], exec
	v_pk_mul_f32 v[96:97], v[96:97], v[170:171] op_sel_hi:[1,0]
	v_pk_mul_f32 v[94:95], v[94:95], v[170:171] op_sel_hi:[1,0]
	v_pk_mul_f32 v[92:93], v[92:93], v[170:171] op_sel_hi:[1,0]
	v_pk_mul_f32 v[90:91], v[90:91], v[170:171] op_sel_hi:[1,0]
	v_pk_mul_f32 v[88:89], v[88:89], v[170:171] op_sel_hi:[1,0]
	v_pk_mul_f32 v[86:87], v[86:87], v[170:171] op_sel_hi:[1,0]
	v_pk_mul_f32 v[84:85], v[84:85], v[170:171] op_sel_hi:[1,0]
	v_pk_mul_f32 v[82:83], v[82:83], v[170:171] op_sel_hi:[1,0]
	v_pk_mul_f32 v[80:81], v[80:81], v[170:171] op_sel_hi:[1,0]
	v_pk_mul_f32 v[78:79], v[78:79], v[170:171] op_sel_hi:[1,0]
	v_pk_mul_f32 v[76:77], v[76:77], v[170:171] op_sel_hi:[1,0]
	v_pk_mul_f32 v[74:75], v[74:75], v[170:171] op_sel_hi:[1,0]
	v_pk_mul_f32 v[72:73], v[72:73], v[170:171] op_sel_hi:[1,0]
	v_pk_mul_f32 v[70:71], v[70:71], v[170:171] op_sel_hi:[1,0]
	v_pk_mul_f32 v[68:69], v[68:69], v[170:171] op_sel_hi:[1,0]
	v_pk_mul_f32 v[66:67], v[66:67], v[170:171] op_sel_hi:[1,0]
	v_add_f32_e32 v168, v168, v160
	v_pk_mul_f32 v[144:145], v[144:145], v[170:171]
	v_pk_mul_f32 v[44:45], v[44:45], v[158:159] op_sel_hi:[1,0]
	v_pk_mul_f32 v[42:43], v[42:43], v[158:159] op_sel_hi:[1,0]
	v_pk_mul_f32 v[28:29], v[28:29], v[158:159] op_sel_hi:[1,0]
	v_pk_mul_f32 v[26:27], v[26:27], v[158:159] op_sel_hi:[1,0]
	v_pk_mul_f32 v[24:25], v[24:25], v[158:159] op_sel_hi:[1,0]
	v_pk_mul_f32 v[22:23], v[22:23], v[158:159] op_sel_hi:[1,0]
	v_pk_mul_f32 v[20:21], v[20:21], v[158:159] op_sel_hi:[1,0]
	v_pk_mul_f32 v[18:19], v[18:19], v[158:159] op_sel_hi:[1,0]
	v_pk_mul_f32 v[16:17], v[16:17], v[158:159] op_sel_hi:[1,0]
	v_pk_mul_f32 v[14:15], v[14:15], v[158:159] op_sel_hi:[1,0]
	v_pk_mul_f32 v[4:5], v[4:5], v[158:159] op_sel_hi:[1,0]
	v_pk_mul_f32 v[2:3], v[2:3], v[158:159] op_sel_hi:[1,0]
	v_pk_mul_f32 v[12:13], v[12:13], v[158:159] op_sel_hi:[1,0]
	v_pk_mul_f32 v[10:11], v[10:11], v[158:159] op_sel_hi:[1,0]
	v_pk_mul_f32 v[8:9], v[8:9], v[158:159] op_sel_hi:[1,0]
	v_pk_mul_f32 v[6:7], v[6:7], v[158:159] op_sel_hi:[1,0]
	v_sub_f32_e32 v106, v106, v160
	v_sub_f32_e32 v107, v107, v160
	v_sub_f32_e32 v108, v108, v160
	v_sub_f32_e32 v109, v109, v160
	v_sub_f32_e32 v114, v114, v160
	v_sub_f32_e32 v115, v115, v160
	v_sub_f32_e32 v116, v116, v160
	v_sub_f32_e32 v117, v117, v160
	v_sub_f32_e32 v122, v122, v160
	v_sub_f32_e32 v123, v123, v160
	v_sub_f32_e32 v124, v124, v160
	v_sub_f32_e32 v125, v125, v160
	v_sub_f32_e32 v126, v126, v160
	v_sub_f32_e32 v127, v127, v160
	v_sub_f32_e32 v128, v128, v160
	v_sub_f32_e32 v129, v129, v160
	s_or_b64 s[46:47], s[46:47], s[52:53]
	s_or_b64 s[44:45], s[44:45], s[48:49]
	s_branch .LBB0_413
